# two lockstep barriers per phase-B block: after the delta read and right before the store burst
# speedup vs baseline: 1.0384x; 1.0009x over previous
.LBB0_3:
	ds_read_b128 v[70:73], v203
	v_add_u32_e32 v132, s12, v220
	s_add_i32 s12, s12, 0x2000000
	v_add_u32_e32 v203, 0x400, v203
	s_cmp_eq_u32 s12, 0x10000000
	s_barrier
	s_waitcnt lgkmcnt(0)
	v_mfma_f32_16x16x32_bf16 v[66:69], v[144:147], v[70:73], 0
	v_add_u32_e32 v133, 0x4000, v132
	v_add_u32_e32 v134, 0x8000, v132
	v_add_u32_e32 v135, 0xc000, v132
	v_mfma_f32_16x16x32_bf16 v[74:77], v[148:151], v[70:73], 0
	v_add_u32_e32 v136, 0x10000, v132
	s_nop 2
	v_exp_f32_e32 v66, v66
	v_exp_f32_e32 v67, v67
	v_mfma_f32_16x16x32_bf16 v[78:81], v[152:155], v[70:73], 0
	v_exp_f32_e32 v68, v68
	v_exp_f32_e32 v69, v69
	v_exp_f32_e32 v74, v74
	v_mfma_f32_16x16x32_bf16 v[82:85], v[156:159], v[70:73], 0
	v_exp_f32_e32 v75, v75
	v_exp_f32_e32 v76, v76
	v_exp_f32_e32 v77, v77
	v_mfma_f32_16x16x32_bf16 v[86:89], v[160:163], v[70:73], 0
	v_exp_f32_e32 v78, v78
	v_exp_f32_e32 v79, v79
	v_exp_f32_e32 v80, v80
	v_mfma_f32_16x16x32_bf16 v[90:93], v[164:167], v[70:73], 0
	v_exp_f32_e32 v81, v81
	v_exp_f32_e32 v82, v82
	v_exp_f32_e32 v83, v83
	v_mfma_f32_16x16x32_bf16 v[94:97], v[168:171], v[70:73], 0
	v_exp_f32_e32 v84, v84
	v_exp_f32_e32 v85, v85
	v_exp_f32_e32 v86, v86
	v_mfma_f32_16x16x32_bf16 v[98:101], v[172:175], v[70:73], 0
	v_exp_f32_e32 v87, v87
	v_exp_f32_e32 v88, v88
	v_exp_f32_e32 v89, v89
	v_mfma_f32_16x16x32_bf16 v[102:105], v[176:179], v[70:73], 0
	v_exp_f32_e32 v90, v90
	v_exp_f32_e32 v91, v91
	v_exp_f32_e32 v92, v92
	v_mfma_f32_16x16x32_bf16 v[108:111], v[180:183], v[70:73], 0
	v_exp_f32_e32 v93, v93
	v_exp_f32_e32 v94, v94
	v_exp_f32_e32 v95, v95
	v_mfma_f32_16x16x32_bf16 v[112:115], v[184:187], v[70:73], 0
	v_exp_f32_e32 v96, v96
	v_exp_f32_e32 v97, v97
	v_exp_f32_e32 v98, v98
	v_mfma_f32_16x16x32_bf16 v[116:119], v[188:191], v[70:73], 0
	v_exp_f32_e32 v99, v99
	v_exp_f32_e32 v100, v100
	v_exp_f32_e32 v101, v101
	v_mfma_f32_16x16x32_bf16 v[120:123], v[232:235], v[70:73], 0
	v_exp_f32_e32 v102, v102
	v_exp_f32_e32 v103, v103
	v_exp_f32_e32 v104, v104
	v_mfma_f32_16x16x32_bf16 v[124:127], v[236:239], v[70:73], 0
	v_exp_f32_e32 v105, v105
	v_exp_f32_e32 v108, v108
	v_exp_f32_e32 v109, v109
	v_mfma_f32_16x16x32_bf16 v[128:131], v[240:243], v[70:73], 0
	v_exp_f32_e32 v110, v110
	v_exp_f32_e32 v111, v111
	v_exp_f32_e32 v112, v112
	v_mfma_f32_16x16x32_bf16 v[70:73], v[244:247], v[70:73], 0
	v_exp_f32_e32 v113, v113
	v_exp_f32_e32 v114, v114
	v_exp_f32_e32 v115, v115
	v_exp_f32_e32 v116, v116
	v_exp_f32_e32 v117, v117
	v_exp_f32_e32 v118, v118
	v_exp_f32_e32 v119, v119
	v_exp_f32_e32 v120, v120
	v_exp_f32_e32 v121, v121
	v_exp_f32_e32 v122, v122
	v_exp_f32_e32 v123, v123
	v_exp_f32_e32 v124, v124
	v_exp_f32_e32 v125, v125
	v_exp_f32_e32 v126, v126
	v_exp_f32_e32 v127, v127
	v_exp_f32_e32 v128, v128
	v_exp_f32_e32 v129, v129
	v_exp_f32_e32 v130, v130
	v_exp_f32_e32 v131, v131
	v_exp_f32_e32 v70, v70
	v_exp_f32_e32 v71, v71
	v_exp_f32_e32 v72, v72
	v_exp_f32_e32 v73, v73
	v_pk_add_f32 v[66:67], v[66:67], 1.0 op_sel_hi:[1,0]
	v_pk_add_f32 v[68:69], v[68:69], 1.0 op_sel_hi:[1,0]
	v_pk_add_f32 v[74:75], v[74:75], 1.0 op_sel_hi:[1,0]
	v_pk_add_f32 v[76:77], v[76:77], 1.0 op_sel_hi:[1,0]
	v_pk_add_f32 v[78:79], v[78:79], 1.0 op_sel_hi:[1,0]
	v_pk_add_f32 v[80:81], v[80:81], 1.0 op_sel_hi:[1,0]
	v_pk_add_f32 v[82:83], v[82:83], 1.0 op_sel_hi:[1,0]
	v_pk_add_f32 v[84:85], v[84:85], 1.0 op_sel_hi:[1,0]
	v_pk_add_f32 v[86:87], v[86:87], 1.0 op_sel_hi:[1,0]
	v_pk_add_f32 v[88:89], v[88:89], 1.0 op_sel_hi:[1,0]
	v_pk_add_f32 v[90:91], v[90:91], 1.0 op_sel_hi:[1,0]
	v_pk_add_f32 v[92:93], v[92:93], 1.0 op_sel_hi:[1,0]
	v_pk_add_f32 v[94:95], v[94:95], 1.0 op_sel_hi:[1,0]
	v_pk_add_f32 v[96:97], v[96:97], 1.0 op_sel_hi:[1,0]
	v_pk_add_f32 v[98:99], v[98:99], 1.0 op_sel_hi:[1,0]
	v_pk_add_f32 v[100:101], v[100:101], 1.0 op_sel_hi:[1,0]
	v_pk_add_f32 v[102:103], v[102:103], 1.0 op_sel_hi:[1,0]
	v_pk_add_f32 v[104:105], v[104:105], 1.0 op_sel_hi:[1,0]
	v_rcp_f32_e32 v66, v66
	v_rcp_f32_e32 v67, v67
	v_rcp_f32_e32 v68, v68
	v_rcp_f32_e32 v69, v69
	v_pk_add_f32 v[108:109], v[108:109], 1.0 op_sel_hi:[1,0]
	v_pk_add_f32 v[110:111], v[110:111], 1.0 op_sel_hi:[1,0]
	v_pk_add_f32 v[112:113], v[112:113], 1.0 op_sel_hi:[1,0]
	v_pk_add_f32 v[114:115], v[114:115], 1.0 op_sel_hi:[1,0]
	v_pk_add_f32 v[116:117], v[116:117], 1.0 op_sel_hi:[1,0]
	v_pk_add_f32 v[118:119], v[118:119], 1.0 op_sel_hi:[1,0]
	v_pk_add_f32 v[120:121], v[120:121], 1.0 op_sel_hi:[1,0]
	v_pk_add_f32 v[122:123], v[122:123], 1.0 op_sel_hi:[1,0]
	v_pk_add_f32 v[124:125], v[124:125], 1.0 op_sel_hi:[1,0]
	v_pk_add_f32 v[126:127], v[126:127], 1.0 op_sel_hi:[1,0]
	v_pk_add_f32 v[128:129], v[128:129], 1.0 op_sel_hi:[1,0]
	v_pk_add_f32 v[130:131], v[130:131], 1.0 op_sel_hi:[1,0]
	v_add_f32_e32 v140, 1.0, v70
	v_add_f32_e32 v141, 1.0, v71
	v_add_f32_e32 v142, 1.0, v72
	v_add_f32_e32 v143, 1.0, v73
	v_rcp_f32_e32 v70, v74
	v_rcp_f32_e32 v71, v75
	v_rcp_f32_e32 v72, v76
	v_rcp_f32_e32 v73, v77
	v_rcp_f32_e32 v74, v78
	v_rcp_f32_e32 v75, v79
	v_rcp_f32_e32 v76, v80
	v_rcp_f32_e32 v77, v81
	v_rcp_f32_e32 v78, v82
	v_rcp_f32_e32 v79, v83
	v_rcp_f32_e32 v80, v84
	v_rcp_f32_e32 v81, v85
	v_rcp_f32_e32 v82, v86
	v_rcp_f32_e32 v83, v87
	v_rcp_f32_e32 v84, v88
	v_rcp_f32_e32 v85, v89
	v_rcp_f32_e32 v86, v90
	v_rcp_f32_e32 v87, v91
	v_rcp_f32_e32 v88, v92
	v_rcp_f32_e32 v89, v93
	v_rcp_f32_e32 v90, v94
	v_rcp_f32_e32 v91, v95
	v_rcp_f32_e32 v92, v96
	v_rcp_f32_e32 v93, v97
	v_rcp_f32_e32 v94, v98
	v_rcp_f32_e32 v95, v99
	v_rcp_f32_e32 v96, v100
	v_rcp_f32_e32 v97, v101
	v_rcp_f32_e32 v98, v102
	v_rcp_f32_e32 v99, v103
	v_rcp_f32_e32 v100, v104
	v_rcp_f32_e32 v101, v105
	v_rcp_f32_e32 v102, v108
	v_rcp_f32_e32 v103, v109
	v_rcp_f32_e32 v104, v110
	v_rcp_f32_e32 v105, v111
	v_rcp_f32_e32 v108, v112
	v_rcp_f32_e32 v109, v113
	v_rcp_f32_e32 v110, v114
	v_rcp_f32_e32 v111, v115
	v_rcp_f32_e32 v112, v116
	v_rcp_f32_e32 v113, v117
	v_rcp_f32_e32 v114, v118
	v_rcp_f32_e32 v115, v119
	v_rcp_f32_e32 v116, v120
	v_rcp_f32_e32 v117, v121
	v_rcp_f32_e32 v118, v122
	v_rcp_f32_e32 v119, v123
	v_rcp_f32_e32 v120, v124
	v_rcp_f32_e32 v121, v125
	v_rcp_f32_e32 v122, v126
	v_rcp_f32_e32 v123, v127
	v_rcp_f32_e32 v124, v128
	v_rcp_f32_e32 v125, v129
	v_rcp_f32_e32 v126, v130
	v_rcp_f32_e32 v127, v131
	v_rcp_f32_e32 v128, v140
	v_rcp_f32_e32 v129, v141
	v_rcp_f32_e32 v130, v142
	v_rcp_f32_e32 v131, v143
	v_pk_fma_f32 v[66:67], v[66:67], -2.0, 1.0 op_sel_hi:[1,0,0]
	v_pk_fma_f32 v[68:69], v[68:69], -2.0, 1.0 op_sel_hi:[1,0,0]
	v_pk_fma_f32 v[70:71], v[70:71], -2.0, 1.0 op_sel_hi:[1,0,0]
	v_pk_fma_f32 v[72:73], v[72:73], -2.0, 1.0 op_sel_hi:[1,0,0]
	v_pk_fma_f32 v[74:75], v[74:75], -2.0, 1.0 op_sel_hi:[1,0,0]
	v_pk_fma_f32 v[76:77], v[76:77], -2.0, 1.0 op_sel_hi:[1,0,0]
	v_pk_fma_f32 v[78:79], v[78:79], -2.0, 1.0 op_sel_hi:[1,0,0]
	v_pk_fma_f32 v[80:81], v[80:81], -2.0, 1.0 op_sel_hi:[1,0,0]
	v_pk_fma_f32 v[82:83], v[82:83], -2.0, 1.0 op_sel_hi:[1,0,0]
	v_pk_fma_f32 v[84:85], v[84:85], -2.0, 1.0 op_sel_hi:[1,0,0]
	v_pk_fma_f32 v[86:87], v[86:87], -2.0, 1.0 op_sel_hi:[1,0,0]
	v_pk_fma_f32 v[88:89], v[88:89], -2.0, 1.0 op_sel_hi:[1,0,0]
	v_pk_fma_f32 v[90:91], v[90:91], -2.0, 1.0 op_sel_hi:[1,0,0]
	v_pk_fma_f32 v[92:93], v[92:93], -2.0, 1.0 op_sel_hi:[1,0,0]
	v_pk_fma_f32 v[94:95], v[94:95], -2.0, 1.0 op_sel_hi:[1,0,0]
	v_pk_fma_f32 v[96:97], v[96:97], -2.0, 1.0 op_sel_hi:[1,0,0]
	v_pk_fma_f32 v[98:99], v[98:99], -2.0, 1.0 op_sel_hi:[1,0,0]
	v_pk_fma_f32 v[100:101], v[100:101], -2.0, 1.0 op_sel_hi:[1,0,0]
	ds_write_b128 v214, v[66:69]
	ds_write_b128 v214, v[70:73] offset:64
	ds_write_b128 v214, v[74:77] offset:128
	ds_write_b128 v214, v[78:81] offset:192
	ds_write_b128 v214, v[82:85] offset:256
	ds_write_b128 v214, v[86:89] offset:320
	ds_write_b128 v214, v[90:93] offset:384
	ds_write_b128 v214, v[94:97] offset:448
	v_pk_fma_f32 v[102:103], v[102:103], -2.0, 1.0 op_sel_hi:[1,0,0]
	v_pk_fma_f32 v[104:105], v[104:105], -2.0, 1.0 op_sel_hi:[1,0,0]
	v_pk_fma_f32 v[108:109], v[108:109], -2.0, 1.0 op_sel_hi:[1,0,0]
	v_pk_fma_f32 v[110:111], v[110:111], -2.0, 1.0 op_sel_hi:[1,0,0]
	v_pk_fma_f32 v[112:113], v[112:113], -2.0, 1.0 op_sel_hi:[1,0,0]
	v_pk_fma_f32 v[114:115], v[114:115], -2.0, 1.0 op_sel_hi:[1,0,0]
	v_pk_fma_f32 v[116:117], v[116:117], -2.0, 1.0 op_sel_hi:[1,0,0]
	v_pk_fma_f32 v[118:119], v[118:119], -2.0, 1.0 op_sel_hi:[1,0,0]
	v_pk_fma_f32 v[120:121], v[120:121], -2.0, 1.0 op_sel_hi:[1,0,0]
	v_pk_fma_f32 v[122:123], v[122:123], -2.0, 1.0 op_sel_hi:[1,0,0]
	v_pk_fma_f32 v[124:125], v[124:125], -2.0, 1.0 op_sel_hi:[1,0,0]
	v_pk_fma_f32 v[126:127], v[126:127], -2.0, 1.0 op_sel_hi:[1,0,0]
	v_pk_fma_f32 v[128:129], v[128:129], -2.0, 1.0 op_sel_hi:[1,0,0]
	v_pk_fma_f32 v[130:131], v[130:131], -2.0, 1.0 op_sel_hi:[1,0,0]
	ds_read_b128 v[66:69], v215
	ds_read_b128 v[70:73], v215 offset:1056
	ds_read_b128 v[74:77], v215 offset:2112
	ds_read_b128 v[78:81], v215 offset:3168
	ds_read_b128 v[82:85], v215 offset:4224
	ds_read_b128 v[86:89], v215 offset:5280
	ds_read_b128 v[90:93], v215 offset:6336
	ds_read_b128 v[94:97], v215 offset:7392
	ds_write_b128 v214, v[98:101]
	ds_write_b128 v214, v[102:105] offset:64
	ds_write_b128 v214, v[108:111] offset:128
	ds_write_b128 v214, v[112:115] offset:192
	ds_write_b128 v214, v[116:119] offset:256
	ds_write_b128 v214, v[120:123] offset:320
	ds_write_b128 v214, v[124:127] offset:384
	ds_write_b128 v214, v[128:131] offset:448
	ds_read_b128 v[98:101], v215
	ds_read_b128 v[102:105], v215 offset:1056
	ds_read_b128 v[108:111], v215 offset:2112
	ds_read_b128 v[112:115], v215 offset:3168
	ds_read_b128 v[116:119], v215 offset:4224
	ds_read_b128 v[120:123], v215 offset:5280
	ds_read_b128 v[124:127], v215 offset:6336
	ds_read_b128 v[128:131], v215 offset:7392
	v_add_u32_e32 v137, 0x14000, v132
	v_add_u32_e32 v138, 0x18000, v132
	v_add_u32_e32 v139, 0x1c000, v132
	s_barrier
	s_waitcnt lgkmcnt(14)
	buffer_store_dwordx4 v[66:69], v132, s[8:11], 0 offen sc0 nt sc1
	buffer_store_dwordx4 v[70:73], v133, s[8:11], 0 offen sc0 nt sc1
	buffer_store_dwordx4 v[74:77], v134, s[8:11], 0 offen sc0 nt sc1
	buffer_store_dwordx4 v[78:81], v135, s[8:11], 0 offen sc0 nt sc1
	buffer_store_dwordx4 v[82:85], v136, s[8:11], 0 offen sc0 nt sc1
	buffer_store_dwordx4 v[86:89], v137, s[8:11], 0 offen sc0 nt sc1
	buffer_store_dwordx4 v[90:93], v138, s[8:11], 0 offen sc0 nt sc1
	buffer_store_dwordx4 v[94:97], v139, s[8:11], 0 offen sc0 nt sc1
	s_waitcnt lgkmcnt(7)
	buffer_store_dwordx4 v[98:101], v132, s[8:11], 0 offen offset:512 sc0 nt sc1
	s_waitcnt lgkmcnt(6)
	buffer_store_dwordx4 v[102:105], v133, s[8:11], 0 offen offset:512 sc0 nt sc1
	s_waitcnt lgkmcnt(5)
	buffer_store_dwordx4 v[108:111], v134, s[8:11], 0 offen offset:512 sc0 nt sc1
	s_waitcnt lgkmcnt(4)
	buffer_store_dwordx4 v[112:115], v135, s[8:11], 0 offen offset:512 sc0 nt sc1
	s_waitcnt lgkmcnt(3)
	buffer_store_dwordx4 v[116:119], v136, s[8:11], 0 offen offset:512 sc0 nt sc1
	s_waitcnt lgkmcnt(2)
	buffer_store_dwordx4 v[120:123], v137, s[8:11], 0 offen offset:512 sc0 nt sc1
	s_waitcnt lgkmcnt(1)
	buffer_store_dwordx4 v[124:127], v138, s[8:11], 0 offen offset:512 sc0 nt sc1
	s_waitcnt lgkmcnt(0)
	buffer_store_dwordx4 v[128:131], v139, s[8:11], 0 offen offset:512 sc0 nt sc1
	s_cbranch_scc0 .LBB0_3
	s_endpgm
